# barrier waits + flush leftovers by waves 1-4, flush fetch by waves 1-3, P13 remap
# speedup vs baseline: 1.0017x; 1.0017x over previous
; __device__ __forceinline__ int lane_id_now() { unsigned z = 0u; asm volatile("" : "+v"(z)); return (int)__builtin_amdgcn_mbcnt_hi(~0u, __builtin_amdgcn_mbcnt_lo(~0u, z)); }
; __device__ __forceinline__ bool cv_one(const CvWork& w) {
;     if (w.wave == 0) return false;
;     int it = __builtin_amdgcn_readfirstlane(w.cur[2 * w.wave]); const int end = __builtin_amdgcn_readfirstlane(w.cur[2 * w.wave + 1]);
;     if (it >= end) {
;         if (it > CV_ITEMS) return false;
;         unsigned base = 0u; if (lane_id_now() == 0) base = __hip_atomic_fetch_add(w.q, (unsigned)CV_BATCH, __ATOMIC_RELAXED, __HIP_MEMORY_SCOPE_AGENT);
;         base = __builtin_amdgcn_readfirstlane(base);
;         if (base >= (unsigned)CV_ITEMS) { w.cur[2 * w.wave] = CV_ITEMS + 1; w.cur[2 * w.wave + 1] = 0; return false; }
;         it = (int)base; w.cur[2 * w.wave + 1] = (int)base + CV_BATCH;
;     }
;     TItem d; { int r = it; const int e = r / CV_I_UP; r -= e * CV_I_UP; const int nb_ = 2 * FF / 32, kb = r / nb_, nbi = r % nb_;
;         d.src = w.wup + (size_t)e * D * 2 * FF + (size_t)(128 * kb) * (2 * FF) + 32 * nbi; d.dst = (bf16*)(w.wup8 + (size_t)e * 2 * FF * D + (size_t)(32 * nbi) * D + 128 * kb);
;         d.gain = w.gain + 128 * kb; d.N = 2 * FF; d.ldk = D; }
;     const int lane = lane_id_now();
;     f32x4 r[16], g[4]; titem8_load<true, true>(d, lane, r, g); titem8_store<true, true>(d, lane, r, g);
;     w.cur[2 * w.wave] = it + 1;
;     return true;
; }
; __device__ __forceinline__ void cv_flush(const CvWork& w) { while (cv_one(w)) {} }
.LBB0_1413:
	s_cmp_eq_u32 s89, 0
	s_cselect_b64 s[0:1], -1, 0
	s_and_b64 vcc, exec, s[0:1]
	s_cbranch_vccnz .LBB0_1430
	s_cmp_gt_u32 s89, 4
	s_cbranch_scc1 .LBB0_1430
	s_lshl_b32 s2, s89, 3
	s_add_i32 s3, s2, 0
	s_add_i32 s2, s3, 0x20180
	v_mov_b32_e32 v2, s2
	s_waitcnt lgkmcnt(0)
	v_mov_b32_e32 v1, 0
	s_mov_b32 s2, 0x10000
	v_mov_b32_e32 v3, 0x10001
	s_add_i32 s3, s3, 0x20184
	s_movk_i32 s12, 0x4000
	s_mov_b32 s13, 0x8000
	s_mov_b32 s14, 0xc000
	s_mov_b32 s15, 0x14000
	s_mov_b32 s16, 0x18000
	s_mov_b32 s17, 0x1c000
	s_mov_b32 s18, 0x20000
	s_mov_b32 s19, 0x24000
	s_mov_b32 s20, 0x28000
	s_mov_b32 s21, 0x2c000
	s_mov_b32 s22, 0x30000
	s_mov_b32 s23, 0x34000
	s_mov_b32 s24, 0x38000
	s_mov_b32 s25, 0x3c000
	s_mov_b32 s26, 0xc3e00000
	s_movk_i32 s27, 0x1000
	v_mov_b32_e32 v4, 0x43e00000
	s_branch .LBB0_1416
